# MoE-up unit switch: expert-id load issued with the row-index loads, one wait instead of two dependent round trips
# speedup vs baseline: 1.0008x; 1.0008x over previous
; #define PG8_LAS __attribute__((address_space(3)))
;     __device__ __forceinline__ size_t boff(const Unit& u) const { return (size_t)__builtin_amdgcn_readfirstlane(panel_e[u.pm]) * estride; }
; #define PG8_SETA(v, u) do { if constexpr (Sched::GATHER) { _Pragma("unroll") for (int h_ = 0; h_ < 2; ++h_) _Pragma("unroll") for (int i_ = 0; i_ < 2; ++i_) { \
;         int R_, C_; stage_rc(tid * 16 + i_ * 8192, R_, C_); int tok_ = S.arow[(u).pm * BM + h_ * HALF + R_]; tok_ = tok_ < 0 ? 0 : tok_; (v)[h_][i_] = (unsigned)(tok_ * K + C_) * 2u; } } } while (0)
; template <class Epi, class Sched, bool ALIGN_EPI = false, bool SP2 = false>
; __device__ __forceinline__ void gemm_phase(PG8_LAS unsigned char* lds, const Gemm g, const Sched& S, const Epi& E) {
;     ...
;         const bool has_next = S.next(ui + 1, nxt);
;         const char* nA = Sched::GATHER ? (const char*)g.A : (has_next ? (const char*)g.A + (size_t)nxt.pm * tstep : cA);
;         if constexpr (Sched::GATHER) { if (has_next) PG8_SETA(vAn, nxt); else { _Pragma("unroll") for (int h_ = 0; h_ < 2; ++h_) { vAn[h_][0] = vAc[h_][0]; vAn[h_][1] = vAc[h_][1]; } }
;             *(PG8_LAS u32x4*)(lds + STAGE_BYTES + tid * 16) = (u32x4){vAn[0][0], vAn[0][1], vAn[1][0], vAn[1][1]}; }     const char* nB = has_next ? (const char*)g.Bt + S.boff(nxt) + (size_t)nxt.pn * tstep : cB;
.LBB13_1439:
	s_nop 0
	v_cndmask_b32_e64 v2, 0, 1, s[8:9]
	v_cmp_ne_u32_e64 s[6:7], 1, v2
	s_andn2_b64 vcc, exec, s[8:9]
	v_mov_b32_e32 v100, v212
	v_mov_b32_e32 v101, v3
	v_mov_b32_e32 v102, v4
	v_mov_b32_e32 v103, v5
	s_cbranch_vccnz .LBB13_1441
	s_mov_b32 s98, s26
	s_ashr_i32 s99, s26, 31
	s_lshl_b64 s[98:99], s[98:99], 2
	s_add_u32 s98, s48, s98
	s_addc_u32 s99, s49, s99
	s_lshl_b32 s2, s26, 8
	v_add_u32_e32 v6, s2, v99
	v_ashrrev_i32_e32 v7, 31, v6
	v_add_u32_e32 v8, s2, v242
	v_lshl_add_u64 v[6:7], v[6:7], 2, s[12:13]
	v_ashrrev_i32_e32 v9, 31, v8
	s_bitset1_b32 s2, 7
	v_lshl_add_u64 v[8:9], v[8:9], 2, s[12:13]
	global_load_dword v2, v[6:7], off
	global_load_dword v10, v[8:9], off
	v_add_u32_e32 v6, s2, v99
	v_ashrrev_i32_e32 v7, 31, v6
	v_add_u32_e32 v8, s2, v242
	v_lshl_add_u64 v[6:7], v[6:7], 2, s[12:13]
	v_ashrrev_i32_e32 v9, 31, v8
	v_lshl_add_u64 v[8:9], v[8:9], 2, s[12:13]
	global_load_dword v6, v[6:7], off
	s_nop 0
	global_load_dword v7, v[8:9], off
	global_load_dword v9, v98, s[98:99]
	s_waitcnt vmcnt(0)
	v_max_i32_e32 v2, 0, v2
	v_max_i32_e32 v8, 0, v10
	v_lshl_add_u32 v100, v2, 11, v241
	v_lshl_add_u32 v101, v8, 11, v243
	v_max_i32_e32 v2, 0, v6
	v_max_i32_e32 v6, 0, v7
	v_lshl_add_u32 v102, v2, 11, v241
	v_lshl_add_u32 v103, v6, 11, v243
.LBB13_1441:
	v_add_u32_e32 v248, s94, v1
	s_and_b64 vcc, exec, s[6:7]
	s_mov_b64 s[8:9], s[34:35]
	ds_write_b128 v248, v[100:103]
	s_cbranch_vccnz .LBB13_1443
	v_readfirstlane_b32 s2, v9
	s_mul_hi_i32 s8, s2, 0xe00000
	s_mul_i32 s2, s2, 0xe00000
	s_add_u32 s2, s53, s2
	s_addc_u32 s27, s58, s8
	s_ashr_i32 s25, s24, 31
	s_lshl_b64 s[8:9], s[24:25], 19
	s_add_u32 s8, s2, s8
	s_addc_u32 s9, s27, s9
